# W_u transposition riders rewritten by hand: 256 blocks x 4 tiles with all loads in flight up front
# speedup vs baseline: 1.0120x; 1.0120x over previous
_Z16gemm_glds_kernelILi2EEvPKDF16_PDF16_PKiS4_S1_S1_PKfiS6_Pc:
	s_load_dword s3, s[0:1], 0x38
	s_mov_b64 s[4:5], -1
	s_waitcnt lgkmcnt(0)
	s_cmp_lt_i32 s2, s3
	s_cbranch_scc1 .LBB2_2
	s_sub_i32 s3, s2, s3
	s_cmp_gt_u32 s3, 255
	s_cbranch_scc1 .LBB2_14
	s_load_dwordx4 s[4:7], s[0:1], 0x40
	v_lshrrev_b32_e32 v1, 8, v0
	v_and_b32_e32 v2, 0xff, v0
	v_and_b32_e32 v3, 63, v0
	v_readfirstlane_b32 s8, v1
	v_bfe_u32 v4, v0, 6, 2
	s_lshl_b32 s9, s3, 1
	s_nop 1
	s_add_u32 s9, s9, s8
	s_lshr_b32 s10, s9, 8
	s_bfe_u32 s11, s9, 0x40004
	s_and_b32 s12, s9, 15
	s_lshl_b32 s13, s11, 6
	s_lshl_b32 s14, s12, 6
	s_mul_i32 s15, s10, 0x3d2844
	s_movk_i32 s24, 0x3e9
	s_waitcnt lgkmcnt(0)
	s_add_u32 s16, s4, s15
	s_addc_u32 s17, s5, 0
	s_add_u32 s18, s16, 0x7a5088
	s_addc_u32 s19, s17, 0
	s_lshl_b32 s15, s10, 21
	s_add_u32 s20, s6, s15
	s_addc_u32 s21, s7, 0
	s_add_u32 s20, s20, 0x800000
	s_addc_u32 s21, s21, 0
	s_add_u32 s22, s20, 0x400000
	s_addc_u32 s23, s21, 0
	v_add_u32_e32 v5, s13, v4
	v_add_u32_e32 v6, s14, v3
	v_cmp_gt_u32_e64 s[28:29], s24, v6
	v_min_u32_e32 v6, 0x3e8, v6
	v_lshlrev_b32_e32 v6, 2, v6
	v_min_u32_e32 v7, 0x3e8, v5
	v_mul_u32_u24_e32 v7, 0xfa4, v7
	v_add_u32_e32 v48, v7, v6
	v_add_u32_e32 v7, 4, v5
	v_min_u32_e32 v7, 0x3e8, v7
	v_mul_u32_u24_e32 v7, 0xfa4, v7
	v_add_u32_e32 v49, v7, v6
	v_add_u32_e32 v7, 8, v5
	v_min_u32_e32 v7, 0x3e8, v7
	v_mul_u32_u24_e32 v7, 0xfa4, v7
	v_add_u32_e32 v50, v7, v6
	v_add_u32_e32 v7, 12, v5
	v_min_u32_e32 v7, 0x3e8, v7
	v_mul_u32_u24_e32 v7, 0xfa4, v7
	v_add_u32_e32 v51, v7, v6
	v_add_u32_e32 v7, 16, v5
	v_min_u32_e32 v7, 0x3e8, v7
	v_mul_u32_u24_e32 v7, 0xfa4, v7
	v_add_u32_e32 v52, v7, v6
	v_add_u32_e32 v7, 20, v5
	v_min_u32_e32 v7, 0x3e8, v7
	v_mul_u32_u24_e32 v7, 0xfa4, v7
	v_add_u32_e32 v53, v7, v6
	v_add_u32_e32 v7, 24, v5
	v_min_u32_e32 v7, 0x3e8, v7
	v_mul_u32_u24_e32 v7, 0xfa4, v7
	v_add_u32_e32 v54, v7, v6
	v_add_u32_e32 v7, 28, v5
	v_min_u32_e32 v7, 0x3e8, v7
	v_mul_u32_u24_e32 v7, 0xfa4, v7
	v_add_u32_e32 v55, v7, v6
	v_add_u32_e32 v7, 32, v5
	v_min_u32_e32 v7, 0x3e8, v7
	v_mul_u32_u24_e32 v7, 0xfa4, v7
	v_add_u32_e32 v56, v7, v6
	v_add_u32_e32 v7, 36, v5
	v_min_u32_e32 v7, 0x3e8, v7
	v_mul_u32_u24_e32 v7, 0xfa4, v7
	v_add_u32_e32 v57, v7, v6
	v_add_u32_e32 v7, 40, v5
	v_min_u32_e32 v7, 0x3e8, v7
	v_mul_u32_u24_e32 v7, 0xfa4, v7
	v_add_u32_e32 v58, v7, v6
	v_add_u32_e32 v7, 44, v5
	v_min_u32_e32 v7, 0x3e8, v7
	v_mul_u32_u24_e32 v7, 0xfa4, v7
	v_add_u32_e32 v59, v7, v6
	v_add_u32_e32 v7, 48, v5
	v_min_u32_e32 v7, 0x3e8, v7
	v_mul_u32_u24_e32 v7, 0xfa4, v7
	v_add_u32_e32 v60, v7, v6
	v_add_u32_e32 v7, 52, v5
	v_min_u32_e32 v7, 0x3e8, v7
	v_mul_u32_u24_e32 v7, 0xfa4, v7
	v_add_u32_e32 v61, v7, v6
	v_add_u32_e32 v7, 56, v5
	v_min_u32_e32 v7, 0x3e8, v7
	v_mul_u32_u24_e32 v7, 0xfa4, v7
	v_add_u32_e32 v62, v7, v6
	v_add_u32_e32 v7, 60, v5
	v_min_u32_e32 v7, 0x3e8, v7
	v_mul_u32_u24_e32 v7, 0xfa4, v7
	v_add_u32_e32 v63, v7, v6
	global_load_dword v16, v48, s[16:17]
	global_load_dword v17, v49, s[16:17]
	global_load_dword v18, v50, s[16:17]
	global_load_dword v19, v51, s[16:17]
	global_load_dword v20, v52, s[16:17]
	global_load_dword v21, v53, s[16:17]
	global_load_dword v22, v54, s[16:17]
	global_load_dword v23, v55, s[16:17]
	global_load_dword v24, v56, s[16:17]
	global_load_dword v25, v57, s[16:17]
	global_load_dword v26, v58, s[16:17]
	global_load_dword v27, v59, s[16:17]
	global_load_dword v28, v60, s[16:17]
	global_load_dword v29, v61, s[16:17]
	global_load_dword v30, v62, s[16:17]
	global_load_dword v31, v63, s[16:17]
	global_load_dword v32, v48, s[18:19]
	global_load_dword v33, v49, s[18:19]
	global_load_dword v34, v50, s[18:19]
	global_load_dword v35, v51, s[18:19]
	global_load_dword v36, v52, s[18:19]
	global_load_dword v37, v53, s[18:19]
	global_load_dword v38, v54, s[18:19]
	global_load_dword v39, v55, s[18:19]
	global_load_dword v40, v56, s[18:19]
	global_load_dword v41, v57, s[18:19]
	global_load_dword v42, v58, s[18:19]
	global_load_dword v43, v59, s[18:19]
	global_load_dword v44, v60, s[18:19]
	global_load_dword v45, v61, s[18:19]
	global_load_dword v46, v62, s[18:19]
	global_load_dword v47, v63, s[18:19]
	v_mul_u32_u24_e32 v8, 65, v4
	v_add_u32_e32 v8, v8, v3
	v_lshlrev_b32_e32 v8, 2, v8
	s_mul_i32 s25, s8, 0x4100
	v_add_u32_e32 v8, s25, v8
	v_and_b32_e32 v9, 7, v2
	v_lshrrev_b32_e32 v10, 3, v2
	v_mul_u32_u24_e32 v11, 0x208, v9
	v_add_u32_e32 v11, v11, v10
	v_lshlrev_b32_e32 v11, 2, v11
	v_add_u32_e32 v11, s25, v11
	v_add_u32_e32 v12, s14, v10
	v_lshlrev_b32_e32 v12, 11, v12
	v_lshlrev_b32_e32 v13, 4, v9
	v_add_u32_e32 v12, v12, v13
	s_lshl_b32 s26, s13, 1
	v_add_u32_e32 v12, s26, v12
	v_add_u32_e32 v14, 0x10000, v12
	s_waitcnt vmcnt(31)
	v_cmp_gt_u32_e32 vcc, s24, v5
	s_and_b64 vcc, vcc, s[28:29]
	s_nop 1
	v_cndmask_b32_e32 v7, 0, v16, vcc
	ds_write_b32 v8, v7
	s_waitcnt vmcnt(30)
	v_add_u32_e32 v7, 4, v5
	v_cmp_gt_u32_e32 vcc, s24, v7
	s_and_b64 vcc, vcc, s[28:29]
	s_nop 1
	v_cndmask_b32_e32 v7, 0, v17, vcc
	ds_write_b32 v8, v7 offset:1040
	s_waitcnt vmcnt(29)
	v_add_u32_e32 v7, 8, v5
	v_cmp_gt_u32_e32 vcc, s24, v7
	s_and_b64 vcc, vcc, s[28:29]
	s_nop 1
	v_cndmask_b32_e32 v7, 0, v18, vcc
	ds_write_b32 v8, v7 offset:2080
	s_waitcnt vmcnt(28)
	v_add_u32_e32 v7, 12, v5
	v_cmp_gt_u32_e32 vcc, s24, v7
	s_and_b64 vcc, vcc, s[28:29]
	s_nop 1
	v_cndmask_b32_e32 v7, 0, v19, vcc
	ds_write_b32 v8, v7 offset:3120
	s_waitcnt vmcnt(27)
	v_add_u32_e32 v7, 16, v5
	v_cmp_gt_u32_e32 vcc, s24, v7
	s_and_b64 vcc, vcc, s[28:29]
	s_nop 1
	v_cndmask_b32_e32 v7, 0, v20, vcc
	ds_write_b32 v8, v7 offset:4160
	s_waitcnt vmcnt(26)
	v_add_u32_e32 v7, 20, v5
	v_cmp_gt_u32_e32 vcc, s24, v7
	s_and_b64 vcc, vcc, s[28:29]
	s_nop 1
	v_cndmask_b32_e32 v7, 0, v21, vcc
	ds_write_b32 v8, v7 offset:5200
	s_waitcnt vmcnt(25)
	v_add_u32_e32 v7, 24, v5
	v_cmp_gt_u32_e32 vcc, s24, v7
	s_and_b64 vcc, vcc, s[28:29]
	s_nop 1
	v_cndmask_b32_e32 v7, 0, v22, vcc
	ds_write_b32 v8, v7 offset:6240
	s_waitcnt vmcnt(24)
	v_add_u32_e32 v7, 28, v5
	v_cmp_gt_u32_e32 vcc, s24, v7
	s_and_b64 vcc, vcc, s[28:29]
	s_nop 1
	v_cndmask_b32_e32 v7, 0, v23, vcc
	ds_write_b32 v8, v7 offset:7280
	s_waitcnt vmcnt(23)
	v_add_u32_e32 v7, 32, v5
	v_cmp_gt_u32_e32 vcc, s24, v7
	s_and_b64 vcc, vcc, s[28:29]
	s_nop 1
	v_cndmask_b32_e32 v7, 0, v24, vcc
	ds_write_b32 v8, v7 offset:8320
	s_waitcnt vmcnt(22)
	v_add_u32_e32 v7, 36, v5
	v_cmp_gt_u32_e32 vcc, s24, v7
	s_and_b64 vcc, vcc, s[28:29]
	s_nop 1
	v_cndmask_b32_e32 v7, 0, v25, vcc
	ds_write_b32 v8, v7 offset:9360
	s_waitcnt vmcnt(21)
	v_add_u32_e32 v7, 40, v5
	v_cmp_gt_u32_e32 vcc, s24, v7
	s_and_b64 vcc, vcc, s[28:29]
	s_nop 1
	v_cndmask_b32_e32 v7, 0, v26, vcc
	ds_write_b32 v8, v7 offset:10400
	s_waitcnt vmcnt(20)
	v_add_u32_e32 v7, 44, v5
	v_cmp_gt_u32_e32 vcc, s24, v7
	s_and_b64 vcc, vcc, s[28:29]
	s_nop 1
	v_cndmask_b32_e32 v7, 0, v27, vcc
	ds_write_b32 v8, v7 offset:11440
	s_waitcnt vmcnt(19)
	v_add_u32_e32 v7, 48, v5
	v_cmp_gt_u32_e32 vcc, s24, v7
	s_and_b64 vcc, vcc, s[28:29]
	s_nop 1
	v_cndmask_b32_e32 v7, 0, v28, vcc
	ds_write_b32 v8, v7 offset:12480
	s_waitcnt vmcnt(18)
	v_add_u32_e32 v7, 52, v5
	v_cmp_gt_u32_e32 vcc, s24, v7
	s_and_b64 vcc, vcc, s[28:29]
	s_nop 1
	v_cndmask_b32_e32 v7, 0, v29, vcc
	ds_write_b32 v8, v7 offset:13520
	s_waitcnt vmcnt(17)
	v_add_u32_e32 v7, 56, v5
	v_cmp_gt_u32_e32 vcc, s24, v7
	s_and_b64 vcc, vcc, s[28:29]
	s_nop 1
	v_cndmask_b32_e32 v7, 0, v30, vcc
	ds_write_b32 v8, v7 offset:14560
	s_waitcnt vmcnt(16)
	v_add_u32_e32 v7, 60, v5
	v_cmp_gt_u32_e32 vcc, s24, v7
	s_and_b64 vcc, vcc, s[28:29]
	s_nop 1
	v_cndmask_b32_e32 v7, 0, v31, vcc
	ds_write_b32 v8, v7 offset:15600
	s_waitcnt lgkmcnt(0)
	s_barrier
	ds_read_b32 v64, v11
	ds_read_b32 v65, v11 offset:260
	ds_read_b32 v66, v11 offset:520
	ds_read_b32 v67, v11 offset:780
	ds_read_b32 v68, v11 offset:1040
	ds_read_b32 v69, v11 offset:1300
	ds_read_b32 v70, v11 offset:1560
	ds_read_b32 v71, v11 offset:1820
	ds_read_b32 v72, v11 offset:128
	ds_read_b32 v73, v11 offset:388
	ds_read_b32 v74, v11 offset:648
	ds_read_b32 v75, v11 offset:908
	s_waitcnt lgkmcnt(4)
	ds_read_b32 v76, v11 offset:1168
	ds_read_b32 v77, v11 offset:1428
	ds_read_b32 v78, v11 offset:1688
	ds_read_b32 v79, v11 offset:1948
	s_waitcnt lgkmcnt(0)
	v_cvt_pk_f16_f32 v80, v64, v65
	v_cvt_pk_f16_f32 v81, v66, v67
	v_cvt_pk_f16_f32 v82, v68, v69
	v_cvt_pk_f16_f32 v83, v70, v71
	v_cvt_pk_f16_f32 v84, v72, v73
	v_cvt_pk_f16_f32 v85, v74, v75
	v_cvt_pk_f16_f32 v86, v76, v77
	v_cvt_pk_f16_f32 v87, v78, v79
	global_store_dwordx4 v12, v[80:83], s[20:21]
	global_store_dwordx4 v14, v[84:87], s[20:21]
	s_barrier
	s_waitcnt vmcnt(17)
	v_cmp_gt_u32_e32 vcc, s24, v5
	s_and_b64 vcc, vcc, s[28:29]
	s_nop 1
	v_cndmask_b32_e32 v7, 0, v32, vcc
	ds_write_b32 v8, v7
	s_waitcnt vmcnt(16)
	v_add_u32_e32 v7, 4, v5
	v_cmp_gt_u32_e32 vcc, s24, v7
	s_and_b64 vcc, vcc, s[28:29]
	s_nop 1
	v_cndmask_b32_e32 v7, 0, v33, vcc
	ds_write_b32 v8, v7 offset:1040
	s_waitcnt vmcnt(15)
	v_add_u32_e32 v7, 8, v5
	v_cmp_gt_u32_e32 vcc, s24, v7
	s_and_b64 vcc, vcc, s[28:29]
	s_nop 1
	v_cndmask_b32_e32 v7, 0, v34, vcc
	ds_write_b32 v8, v7 offset:2080
	s_waitcnt vmcnt(14)
	v_add_u32_e32 v7, 12, v5
	v_cmp_gt_u32_e32 vcc, s24, v7
	s_and_b64 vcc, vcc, s[28:29]
	s_nop 1
	v_cndmask_b32_e32 v7, 0, v35, vcc
	ds_write_b32 v8, v7 offset:3120
	s_waitcnt vmcnt(13)
	v_add_u32_e32 v7, 16, v5
	v_cmp_gt_u32_e32 vcc, s24, v7
	s_and_b64 vcc, vcc, s[28:29]
	s_nop 1
	v_cndmask_b32_e32 v7, 0, v36, vcc
	ds_write_b32 v8, v7 offset:4160
	s_waitcnt vmcnt(12)
	v_add_u32_e32 v7, 20, v5
	v_cmp_gt_u32_e32 vcc, s24, v7
	s_and_b64 vcc, vcc, s[28:29]
	s_nop 1
	v_cndmask_b32_e32 v7, 0, v37, vcc
	ds_write_b32 v8, v7 offset:5200
	s_waitcnt vmcnt(11)
	v_add_u32_e32 v7, 24, v5
	v_cmp_gt_u32_e32 vcc, s24, v7
	s_and_b64 vcc, vcc, s[28:29]
	s_nop 1
	v_cndmask_b32_e32 v7, 0, v38, vcc
	ds_write_b32 v8, v7 offset:6240
	s_waitcnt vmcnt(10)
	v_add_u32_e32 v7, 28, v5
	v_cmp_gt_u32_e32 vcc, s24, v7
	s_and_b64 vcc, vcc, s[28:29]
	s_nop 1
	v_cndmask_b32_e32 v7, 0, v39, vcc
	ds_write_b32 v8, v7 offset:7280
	s_waitcnt vmcnt(9)
	v_add_u32_e32 v7, 32, v5
	v_cmp_gt_u32_e32 vcc, s24, v7
	s_and_b64 vcc, vcc, s[28:29]
	s_nop 1
	v_cndmask_b32_e32 v7, 0, v40, vcc
	ds_write_b32 v8, v7 offset:8320
	s_waitcnt vmcnt(8)
	v_add_u32_e32 v7, 36, v5
	v_cmp_gt_u32_e32 vcc, s24, v7
	s_and_b64 vcc, vcc, s[28:29]
	s_nop 1
	v_cndmask_b32_e32 v7, 0, v41, vcc
	ds_write_b32 v8, v7 offset:9360
	s_waitcnt vmcnt(7)
	v_add_u32_e32 v7, 40, v5
	v_cmp_gt_u32_e32 vcc, s24, v7
	s_and_b64 vcc, vcc, s[28:29]
	s_nop 1
	v_cndmask_b32_e32 v7, 0, v42, vcc
	ds_write_b32 v8, v7 offset:10400
	s_waitcnt vmcnt(6)
	v_add_u32_e32 v7, 44, v5
	v_cmp_gt_u32_e32 vcc, s24, v7
	s_and_b64 vcc, vcc, s[28:29]
	s_nop 1
	v_cndmask_b32_e32 v7, 0, v43, vcc
	ds_write_b32 v8, v7 offset:11440
	s_waitcnt vmcnt(5)
	v_add_u32_e32 v7, 48, v5
	v_cmp_gt_u32_e32 vcc, s24, v7
	s_and_b64 vcc, vcc, s[28:29]
	s_nop 1
	v_cndmask_b32_e32 v7, 0, v44, vcc
	ds_write_b32 v8, v7 offset:12480
	s_waitcnt vmcnt(4)
	v_add_u32_e32 v7, 52, v5
	v_cmp_gt_u32_e32 vcc, s24, v7
	s_and_b64 vcc, vcc, s[28:29]
	s_nop 1
	v_cndmask_b32_e32 v7, 0, v45, vcc
	ds_write_b32 v8, v7 offset:13520
	s_waitcnt vmcnt(3)
	v_add_u32_e32 v7, 56, v5
	v_cmp_gt_u32_e32 vcc, s24, v7
	s_and_b64 vcc, vcc, s[28:29]
	s_nop 1
	v_cndmask_b32_e32 v7, 0, v46, vcc
	ds_write_b32 v8, v7 offset:14560
	s_waitcnt vmcnt(2)
	v_add_u32_e32 v7, 60, v5
	v_cmp_gt_u32_e32 vcc, s24, v7
	s_and_b64 vcc, vcc, s[28:29]
	s_nop 1
	v_cndmask_b32_e32 v7, 0, v47, vcc
	ds_write_b32 v8, v7 offset:15600
	s_waitcnt lgkmcnt(0)
	s_barrier
	ds_read_b32 v64, v11
	ds_read_b32 v65, v11 offset:260
	ds_read_b32 v66, v11 offset:520
	ds_read_b32 v67, v11 offset:780
	ds_read_b32 v68, v11 offset:1040
	ds_read_b32 v69, v11 offset:1300
	ds_read_b32 v70, v11 offset:1560
	ds_read_b32 v71, v11 offset:1820
	ds_read_b32 v72, v11 offset:128
	ds_read_b32 v73, v11 offset:388
	ds_read_b32 v74, v11 offset:648
	ds_read_b32 v75, v11 offset:908
	s_waitcnt lgkmcnt(4)
	ds_read_b32 v76, v11 offset:1168
	ds_read_b32 v77, v11 offset:1428
	ds_read_b32 v78, v11 offset:1688
	ds_read_b32 v79, v11 offset:1948
	s_waitcnt lgkmcnt(0)
	v_cvt_pk_f16_f32 v80, v64, v65
	v_cvt_pk_f16_f32 v81, v66, v67
	v_cvt_pk_f16_f32 v82, v68, v69
	v_cvt_pk_f16_f32 v83, v70, v71
	v_cvt_pk_f16_f32 v84, v72, v73
	v_cvt_pk_f16_f32 v85, v74, v75
	v_cvt_pk_f16_f32 v86, v76, v77
	v_cvt_pk_f16_f32 v87, v78, v79
	global_store_dwordx4 v12, v[80:83], s[22:23]
	global_store_dwordx4 v14, v[84:87], s[22:23]
	s_branch .LBB2_14
